# k8 plus in-projection rope epilogue with 3-deep prefetch of the rope-table rows
# baseline (speedup 1.0000x reference)
.LBB0_132:
	v_ashrrev_i32_e32 v159, 31, v158
	v_lshlrev_b64 v[228:229], 8, v[158:159]
	v_lshl_add_u64 v[228:229], v[148:149], 0, v[228:229]
	global_load_dwordx4 v[204:207], v[228:229], off offset:16
	global_load_dwordx4 v[208:211], v[228:229], off
	v_lshlrev_b64 v[228:229], 8, v[158:159]
	v_lshl_add_u64 v[228:229], v[148:149], 0, v[228:229]
	s_mov_b32 s98, 0x1000
	s_mov_b32 s99, 0
	v_lshl_add_u64 v[228:229], v[228:229], 0, s[98:99]
	global_load_dwordx4 v[212:215], v[228:229], off offset:16
	global_load_dwordx4 v[216:219], v[228:229], off
	v_lshlrev_b64 v[228:229], 8, v[158:159]
	v_lshl_add_u64 v[228:229], v[148:149], 0, v[228:229]
	s_mov_b32 s98, 0x2000
	s_mov_b32 s99, 0
	v_lshl_add_u64 v[228:229], v[228:229], 0, s[98:99]
	global_load_dwordx4 v[220:223], v[228:229], off offset:16
	global_load_dwordx4 v[224:227], v[228:229], off
	v_lshlrev_b64 v[172:173], 8, v[158:159]
	v_lshl_add_u64 v[172:173], v[148:149], 0, v[172:173]
	s_nop 0
	s_nop 0
	s_cmp_lt_u32 s44, 17
	s_cselect_b64 vcc, -1, 0
	s_and_b64 s[28:29], vcc, exec
	s_mov_b32 s21, 0x48400000
	s_cselect_b32 s21, s21, 0x49400000
	s_cselect_b32 s11, -13, 0xffffffef
	s_add_u32 s21, s94, s21
	s_addc_u32 s30, s95, 0
	s_add_i32 s11, s11, s44
	s_lshl_b32 s28, s11, 8
	s_ashr_i32 s29, s28, 31
	s_lshl_b64 s[28:29], s[28:29], 1
	s_add_u32 s28, s21, s28
	v_cndmask_b32_e32 v130, 1.0, v184, vcc
	s_addc_u32 s29, s30, s29
	v_lshl_add_u64 v[132:133], s[28:29], 0, v[144:145]
	v_lshlrev_b64 v[172:173], 11, v[158:159]
	v_lshl_add_u64 v[172:173], v[132:133], 0, v[172:173]
	v_ashrrev_i32_e32 v171, 31, v170
	v_ashrrev_i32_e32 v169, 31, v168
	v_ashrrev_i32_e32 v167, 31, v166
	v_ashrrev_i32_e32 v165, 31, v164
	v_ashrrev_i32_e32 v163, 31, v162
	v_ashrrev_i32_e32 v161, 31, v160
	s_waitcnt vmcnt(4)
	v_mov_b32_e32 v186, v204
	v_mov_b32_e32 v187, v205
	v_mov_b32_e32 v188, v206
	v_mov_b32_e32 v189, v207
	v_mov_b32_e32 v190, v208
	v_mov_b32_e32 v191, v209
	v_mov_b32_e32 v192, v210
	v_mov_b32_e32 v193, v211
	v_lshlrev_b64 v[228:229], 8, v[158:159]
	v_lshl_add_u64 v[228:229], v[148:149], 0, v[228:229]
	s_mov_b32 s98, 0x3000
	s_mov_b32 s99, 0
	v_lshl_add_u64 v[228:229], v[228:229], 0, s[98:99]
	global_load_dwordx4 v[204:207], v[228:229], off offset:16
	global_load_dwordx4 v[208:211], v[228:229], off
	v_mov_b32_e32 v196, v187
	v_mov_b32_e32 v197, v189
	v_mov_b32_e32 v198, v191
	v_mov_b32_e32 v199, v193
	v_pk_mul_f32 v[194:195], v[124:125], v[196:197]
	v_pk_mul_f32 v[200:201], v[122:123], v[198:199]
	v_mov_b32_e32 v191, v192
	v_mov_b32_e32 v187, v188
	v_pk_fma_f32 v[192:193], v[126:127], v[190:191], v[200:201] neg_lo:[0,0,1] neg_hi:[0,0,1]
	v_pk_fma_f32 v[188:189], v[128:129], v[186:187], v[194:195] neg_lo:[0,0,1] neg_hi:[0,0,1]
	v_pk_mul_f32 v[194:195], v[124:125], v[186:187]
	v_pk_mul_f32 v[200:201], v[122:123], v[190:191]
	v_pk_mul_f32 v[192:193], v[130:131], v[192:193] op_sel_hi:[0,1]
	v_pk_fma_f32 v[200:201], v[126:127], v[198:199], v[200:201]
	v_pk_fma_f32 v[194:195], v[128:129], v[196:197], v[194:195]
	v_pk_mul_f32 v[188:189], v[130:131], v[188:189] op_sel_hi:[0,1]
	v_pk_mul_f32 v[202:203], v[130:131], v[194:195] op_sel_hi:[0,1]
	v_pk_mul_f32 v[194:195], v[130:131], v[200:201] op_sel_hi:[0,1]
	v_cvt_pk_bf16_f32 v192, v192, v193
	v_cvt_pk_bf16_f32 v193, v188, v189
	v_cvt_pk_bf16_f32 v194, v194, v195
	v_cvt_pk_bf16_f32 v195, v202, v203
	global_store_dwordx4 v[172:173], v[192:195], off
	v_pk_mul_f32 v[188:189], v[108:109], v[196:197]
	s_nop 0
	v_pk_mul_f32 v[192:193], v[106:107], v[198:199]
	v_pk_fma_f32 v[188:189], v[116:117], v[186:187], v[188:189] neg_lo:[0,0,1] neg_hi:[0,0,1]
	v_pk_fma_f32 v[192:193], v[114:115], v[190:191], v[192:193] neg_lo:[0,0,1] neg_hi:[0,0,1]
	v_pk_mul_f32 v[186:187], v[108:109], v[186:187]
	v_pk_mul_f32 v[190:191], v[106:107], v[190:191]
	v_pk_mul_f32 v[188:189], v[130:131], v[188:189] op_sel_hi:[0,1]
	v_pk_fma_f32 v[190:191], v[114:115], v[198:199], v[190:191]
	v_pk_fma_f32 v[186:187], v[116:117], v[196:197], v[186:187]
	v_pk_mul_f32 v[192:193], v[130:131], v[192:193] op_sel_hi:[0,1]
	v_pk_mul_f32 v[194:195], v[130:131], v[186:187] op_sel_hi:[0,1]
	v_pk_mul_f32 v[190:191], v[130:131], v[190:191] op_sel_hi:[0,1]
	v_cvt_pk_bf16_f32 v186, v192, v193
	v_cvt_pk_bf16_f32 v187, v188, v189
	v_cvt_pk_bf16_f32 v188, v190, v191
	v_cvt_pk_bf16_f32 v189, v194, v195
	global_store_dwordx4 v[172:173], v[186:189], off offset:256
	v_lshlrev_b64 v[172:173], 8, v[170:171]
	v_lshl_add_u64 v[172:173], v[148:149], 0, v[172:173]
	s_nop 0
	s_nop 0
	v_lshlrev_b64 v[172:173], 11, v[170:171]
	v_lshl_add_u64 v[172:173], v[132:133], 0, v[172:173]
	s_waitcnt vmcnt(4)
	v_mov_b32_e32 v186, v212
	v_mov_b32_e32 v187, v213
	v_mov_b32_e32 v188, v214
	v_mov_b32_e32 v189, v215
	v_mov_b32_e32 v190, v216
	v_mov_b32_e32 v191, v217
	v_mov_b32_e32 v192, v218
	v_mov_b32_e32 v193, v219
	v_lshlrev_b64 v[228:229], 8, v[158:159]
	v_lshl_add_u64 v[228:229], v[148:149], 0, v[228:229]
	s_mov_b32 s98, 0x8000
	s_mov_b32 s99, 0
	v_lshl_add_u64 v[228:229], v[228:229], 0, s[98:99]
	global_load_dwordx4 v[212:215], v[228:229], off offset:16
	global_load_dwordx4 v[216:219], v[228:229], off
	v_mov_b32_e32 v196, v187
	v_mov_b32_e32 v197, v189
	v_mov_b32_e32 v198, v191
	v_mov_b32_e32 v199, v193
	v_pk_mul_f32 v[194:195], v[112:113], v[196:197]
	v_pk_mul_f32 v[200:201], v[110:111], v[198:199]
	v_mov_b32_e32 v191, v192
	v_mov_b32_e32 v187, v188
	v_pk_fma_f32 v[192:193], v[118:119], v[190:191], v[200:201] neg_lo:[0,0,1] neg_hi:[0,0,1]
	v_pk_fma_f32 v[188:189], v[120:121], v[186:187], v[194:195] neg_lo:[0,0,1] neg_hi:[0,0,1]
	v_pk_mul_f32 v[194:195], v[112:113], v[186:187]
	v_pk_mul_f32 v[200:201], v[110:111], v[190:191]
	v_pk_mul_f32 v[192:193], v[130:131], v[192:193] op_sel_hi:[0,1]
	v_pk_fma_f32 v[200:201], v[118:119], v[198:199], v[200:201]
	v_pk_fma_f32 v[194:195], v[120:121], v[196:197], v[194:195]
	v_pk_mul_f32 v[188:189], v[130:131], v[188:189] op_sel_hi:[0,1]
	v_pk_mul_f32 v[202:203], v[130:131], v[194:195] op_sel_hi:[0,1]
	v_pk_mul_f32 v[194:195], v[130:131], v[200:201] op_sel_hi:[0,1]
	v_cvt_pk_bf16_f32 v192, v192, v193
	v_cvt_pk_bf16_f32 v193, v188, v189
	v_cvt_pk_bf16_f32 v194, v194, v195
	v_cvt_pk_bf16_f32 v195, v202, v203
	global_store_dwordx4 v[172:173], v[192:195], off
	v_pk_mul_f32 v[188:189], v[92:93], v[196:197]
	s_nop 0
	v_pk_mul_f32 v[192:193], v[90:91], v[198:199]
	v_pk_fma_f32 v[188:189], v[100:101], v[186:187], v[188:189] neg_lo:[0,0,1] neg_hi:[0,0,1]
	v_pk_fma_f32 v[192:193], v[98:99], v[190:191], v[192:193] neg_lo:[0,0,1] neg_hi:[0,0,1]
	v_pk_mul_f32 v[186:187], v[92:93], v[186:187]
	v_pk_mul_f32 v[190:191], v[90:91], v[190:191]
	v_pk_mul_f32 v[188:189], v[130:131], v[188:189] op_sel_hi:[0,1]
	v_pk_fma_f32 v[190:191], v[98:99], v[198:199], v[190:191]
	v_pk_fma_f32 v[186:187], v[100:101], v[196:197], v[186:187]
	v_pk_mul_f32 v[192:193], v[130:131], v[192:193] op_sel_hi:[0,1]
	v_pk_mul_f32 v[194:195], v[130:131], v[186:187] op_sel_hi:[0,1]
	v_pk_mul_f32 v[190:191], v[130:131], v[190:191] op_sel_hi:[0,1]
	v_cvt_pk_bf16_f32 v186, v192, v193
	v_cvt_pk_bf16_f32 v187, v188, v189
	v_cvt_pk_bf16_f32 v188, v190, v191
	v_cvt_pk_bf16_f32 v189, v194, v195
	global_store_dwordx4 v[172:173], v[186:189], off offset:256
	v_lshlrev_b64 v[172:173], 8, v[168:169]
	v_lshl_add_u64 v[172:173], v[148:149], 0, v[172:173]
	s_nop 0
	s_nop 0
	v_lshlrev_b64 v[172:173], 11, v[168:169]
	v_lshl_add_u64 v[172:173], v[132:133], 0, v[172:173]
	s_waitcnt vmcnt(4)
	v_mov_b32_e32 v186, v220
	v_mov_b32_e32 v187, v221
	v_mov_b32_e32 v188, v222
	v_mov_b32_e32 v189, v223
	v_mov_b32_e32 v190, v224
	v_mov_b32_e32 v191, v225
	v_mov_b32_e32 v192, v226
	v_mov_b32_e32 v193, v227
	v_lshlrev_b64 v[228:229], 8, v[158:159]
	v_lshl_add_u64 v[228:229], v[148:149], 0, v[228:229]
	s_mov_b32 s98, 0x9000
	s_mov_b32 s99, 0
	v_lshl_add_u64 v[228:229], v[228:229], 0, s[98:99]
	global_load_dwordx4 v[220:223], v[228:229], off offset:16
	global_load_dwordx4 v[224:227], v[228:229], off
	v_mov_b32_e32 v196, v187
	v_mov_b32_e32 v197, v189
	v_mov_b32_e32 v198, v191
	v_mov_b32_e32 v199, v193
	v_pk_mul_f32 v[194:195], v[96:97], v[196:197]
	v_pk_mul_f32 v[200:201], v[94:95], v[198:199]
	v_mov_b32_e32 v191, v192
	v_mov_b32_e32 v187, v188
	v_pk_fma_f32 v[192:193], v[102:103], v[190:191], v[200:201] neg_lo:[0,0,1] neg_hi:[0,0,1]
	v_pk_fma_f32 v[188:189], v[104:105], v[186:187], v[194:195] neg_lo:[0,0,1] neg_hi:[0,0,1]
	v_pk_mul_f32 v[194:195], v[96:97], v[186:187]
	v_pk_mul_f32 v[200:201], v[94:95], v[190:191]
	v_pk_mul_f32 v[192:193], v[130:131], v[192:193] op_sel_hi:[0,1]
	v_pk_fma_f32 v[200:201], v[102:103], v[198:199], v[200:201]
	v_pk_fma_f32 v[194:195], v[104:105], v[196:197], v[194:195]
	v_pk_mul_f32 v[188:189], v[130:131], v[188:189] op_sel_hi:[0,1]
	v_pk_mul_f32 v[202:203], v[130:131], v[194:195] op_sel_hi:[0,1]
	v_pk_mul_f32 v[194:195], v[130:131], v[200:201] op_sel_hi:[0,1]
	v_cvt_pk_bf16_f32 v192, v192, v193
	v_cvt_pk_bf16_f32 v193, v188, v189
	v_cvt_pk_bf16_f32 v194, v194, v195
	v_cvt_pk_bf16_f32 v195, v202, v203
	global_store_dwordx4 v[172:173], v[192:195], off
	v_pk_mul_f32 v[188:189], v[76:77], v[196:197]
	s_nop 0
	v_pk_mul_f32 v[192:193], v[74:75], v[198:199]
	v_pk_fma_f32 v[188:189], v[84:85], v[186:187], v[188:189] neg_lo:[0,0,1] neg_hi:[0,0,1]
	v_pk_fma_f32 v[192:193], v[82:83], v[190:191], v[192:193] neg_lo:[0,0,1] neg_hi:[0,0,1]
	v_pk_mul_f32 v[186:187], v[76:77], v[186:187]
	v_pk_mul_f32 v[190:191], v[74:75], v[190:191]
	v_pk_mul_f32 v[188:189], v[130:131], v[188:189] op_sel_hi:[0,1]
	v_pk_fma_f32 v[190:191], v[82:83], v[198:199], v[190:191]
	v_pk_fma_f32 v[186:187], v[84:85], v[196:197], v[186:187]
	v_pk_mul_f32 v[192:193], v[130:131], v[192:193] op_sel_hi:[0,1]
	v_pk_mul_f32 v[194:195], v[130:131], v[186:187] op_sel_hi:[0,1]
	v_pk_mul_f32 v[190:191], v[130:131], v[190:191] op_sel_hi:[0,1]
	v_cvt_pk_bf16_f32 v186, v192, v193
	v_cvt_pk_bf16_f32 v187, v188, v189
	v_cvt_pk_bf16_f32 v188, v190, v191
	v_cvt_pk_bf16_f32 v189, v194, v195
	global_store_dwordx4 v[172:173], v[186:189], off offset:256
	v_lshlrev_b64 v[172:173], 8, v[166:167]
	v_lshl_add_u64 v[172:173], v[148:149], 0, v[172:173]
	s_nop 0
	s_nop 0
	v_lshlrev_b64 v[172:173], 11, v[166:167]
	v_lshl_add_u64 v[172:173], v[132:133], 0, v[172:173]
	s_waitcnt vmcnt(4)
	v_mov_b32_e32 v186, v204
	v_mov_b32_e32 v187, v205
	v_mov_b32_e32 v188, v206
	v_mov_b32_e32 v189, v207
	v_mov_b32_e32 v190, v208
	v_mov_b32_e32 v191, v209
	v_mov_b32_e32 v192, v210
	v_mov_b32_e32 v193, v211
	v_lshlrev_b64 v[228:229], 8, v[158:159]
	v_lshl_add_u64 v[228:229], v[148:149], 0, v[228:229]
	s_mov_b32 s98, 0xa000
	s_mov_b32 s99, 0
	v_lshl_add_u64 v[228:229], v[228:229], 0, s[98:99]
	global_load_dwordx4 v[204:207], v[228:229], off offset:16
	global_load_dwordx4 v[208:211], v[228:229], off
	v_mov_b32_e32 v196, v187
	v_mov_b32_e32 v197, v189
	v_mov_b32_e32 v198, v191
	v_mov_b32_e32 v199, v193
	v_pk_mul_f32 v[194:195], v[80:81], v[196:197]
	v_pk_mul_f32 v[200:201], v[78:79], v[198:199]
	v_mov_b32_e32 v191, v192
	v_mov_b32_e32 v187, v188
	v_pk_fma_f32 v[192:193], v[86:87], v[190:191], v[200:201] neg_lo:[0,0,1] neg_hi:[0,0,1]
	v_pk_fma_f32 v[188:189], v[88:89], v[186:187], v[194:195] neg_lo:[0,0,1] neg_hi:[0,0,1]
	v_pk_mul_f32 v[194:195], v[80:81], v[186:187]
	v_pk_mul_f32 v[200:201], v[78:79], v[190:191]
	v_pk_mul_f32 v[192:193], v[130:131], v[192:193] op_sel_hi:[0,1]
	v_pk_fma_f32 v[200:201], v[86:87], v[198:199], v[200:201]
	v_pk_fma_f32 v[194:195], v[88:89], v[196:197], v[194:195]
	v_pk_mul_f32 v[188:189], v[130:131], v[188:189] op_sel_hi:[0,1]
	v_pk_mul_f32 v[202:203], v[130:131], v[194:195] op_sel_hi:[0,1]
	v_pk_mul_f32 v[194:195], v[130:131], v[200:201] op_sel_hi:[0,1]
	v_cvt_pk_bf16_f32 v192, v192, v193
	v_cvt_pk_bf16_f32 v193, v188, v189
	v_cvt_pk_bf16_f32 v194, v194, v195
	v_cvt_pk_bf16_f32 v195, v202, v203
	global_store_dwordx4 v[172:173], v[192:195], off
	v_pk_mul_f32 v[188:189], v[68:69], v[196:197]
	s_nop 0
	v_pk_mul_f32 v[192:193], v[66:67], v[198:199]
	v_pk_fma_f32 v[188:189], v[72:73], v[186:187], v[188:189] neg_lo:[0,0,1] neg_hi:[0,0,1]
	v_pk_fma_f32 v[192:193], v[70:71], v[190:191], v[192:193] neg_lo:[0,0,1] neg_hi:[0,0,1]
	v_pk_mul_f32 v[186:187], v[68:69], v[186:187]
	v_pk_mul_f32 v[190:191], v[66:67], v[190:191]
	v_pk_mul_f32 v[188:189], v[130:131], v[188:189] op_sel_hi:[0,1]
	v_pk_fma_f32 v[190:191], v[70:71], v[198:199], v[190:191]
	v_pk_fma_f32 v[186:187], v[72:73], v[196:197], v[186:187]
	v_pk_mul_f32 v[192:193], v[130:131], v[192:193] op_sel_hi:[0,1]
	v_pk_mul_f32 v[194:195], v[130:131], v[186:187] op_sel_hi:[0,1]
	v_pk_mul_f32 v[190:191], v[130:131], v[190:191] op_sel_hi:[0,1]
	v_cvt_pk_bf16_f32 v186, v192, v193
	v_cvt_pk_bf16_f32 v187, v188, v189
	v_cvt_pk_bf16_f32 v188, v190, v191
	v_cvt_pk_bf16_f32 v189, v194, v195
	global_store_dwordx4 v[172:173], v[186:189], off offset:256
	v_lshlrev_b64 v[172:173], 8, v[164:165]
	v_lshl_add_u64 v[172:173], v[148:149], 0, v[172:173]
	s_nop 0
	s_nop 0
	v_lshlrev_b64 v[172:173], 11, v[164:165]
	v_lshl_add_u64 v[172:173], v[132:133], 0, v[172:173]
	s_waitcnt vmcnt(4)
	v_mov_b32_e32 v186, v212
	v_mov_b32_e32 v187, v213
	v_mov_b32_e32 v188, v214
	v_mov_b32_e32 v189, v215
	v_mov_b32_e32 v190, v216
	v_mov_b32_e32 v191, v217
	v_mov_b32_e32 v192, v218
	v_mov_b32_e32 v193, v219
	v_lshlrev_b64 v[228:229], 8, v[158:159]
	v_lshl_add_u64 v[228:229], v[148:149], 0, v[228:229]
	s_mov_b32 s98, 0xb000
	s_mov_b32 s99, 0
	v_lshl_add_u64 v[228:229], v[228:229], 0, s[98:99]
	global_load_dwordx4 v[212:215], v[228:229], off offset:16
	global_load_dwordx4 v[216:219], v[228:229], off
	v_mov_b32_e32 v196, v187
	v_mov_b32_e32 v197, v189
	v_mov_b32_e32 v198, v191
	v_mov_b32_e32 v199, v193
	v_pk_mul_f32 v[194:195], v[60:61], v[196:197]
	v_pk_mul_f32 v[200:201], v[58:59], v[198:199]
	v_mov_b32_e32 v191, v192
	v_mov_b32_e32 v187, v188
	v_pk_fma_f32 v[192:193], v[62:63], v[190:191], v[200:201] neg_lo:[0,0,1] neg_hi:[0,0,1]
	v_pk_fma_f32 v[188:189], v[64:65], v[186:187], v[194:195] neg_lo:[0,0,1] neg_hi:[0,0,1]
	v_pk_mul_f32 v[194:195], v[60:61], v[186:187]
	v_pk_mul_f32 v[200:201], v[58:59], v[190:191]
	v_pk_mul_f32 v[192:193], v[130:131], v[192:193] op_sel_hi:[0,1]
	v_pk_fma_f32 v[200:201], v[62:63], v[198:199], v[200:201]
	v_pk_fma_f32 v[194:195], v[64:65], v[196:197], v[194:195]
	v_pk_mul_f32 v[188:189], v[130:131], v[188:189] op_sel_hi:[0,1]
	v_pk_mul_f32 v[202:203], v[130:131], v[194:195] op_sel_hi:[0,1]
	v_pk_mul_f32 v[194:195], v[130:131], v[200:201] op_sel_hi:[0,1]
	v_cvt_pk_bf16_f32 v192, v192, v193
	v_cvt_pk_bf16_f32 v193, v188, v189
	v_cvt_pk_bf16_f32 v194, v194, v195
	v_cvt_pk_bf16_f32 v195, v202, v203
	global_store_dwordx4 v[172:173], v[192:195], off
	v_pk_mul_f32 v[188:189], v[44:45], v[196:197]
	s_nop 0
	v_pk_mul_f32 v[192:193], v[42:43], v[198:199]
	v_pk_fma_f32 v[188:189], v[52:53], v[186:187], v[188:189] neg_lo:[0,0,1] neg_hi:[0,0,1]
	v_pk_fma_f32 v[192:193], v[50:51], v[190:191], v[192:193] neg_lo:[0,0,1] neg_hi:[0,0,1]
	v_pk_mul_f32 v[186:187], v[44:45], v[186:187]
	v_pk_mul_f32 v[190:191], v[42:43], v[190:191]
	v_pk_mul_f32 v[188:189], v[130:131], v[188:189] op_sel_hi:[0,1]
	v_pk_fma_f32 v[190:191], v[50:51], v[198:199], v[190:191]
	v_pk_fma_f32 v[186:187], v[52:53], v[196:197], v[186:187]
	v_pk_mul_f32 v[192:193], v[130:131], v[192:193] op_sel_hi:[0,1]
	v_pk_mul_f32 v[194:195], v[130:131], v[186:187] op_sel_hi:[0,1]
	v_pk_mul_f32 v[190:191], v[130:131], v[190:191] op_sel_hi:[0,1]
	v_cvt_pk_bf16_f32 v186, v192, v193
	v_cvt_pk_bf16_f32 v187, v188, v189
	v_cvt_pk_bf16_f32 v188, v190, v191
	v_cvt_pk_bf16_f32 v189, v194, v195
	global_store_dwordx4 v[172:173], v[186:189], off offset:256
	v_lshlrev_b64 v[172:173], 8, v[162:163]
	v_lshl_add_u64 v[172:173], v[148:149], 0, v[172:173]
	s_nop 0
	s_nop 0
	v_lshlrev_b64 v[172:173], 11, v[162:163]
	v_lshl_add_u64 v[172:173], v[132:133], 0, v[172:173]
	s_waitcnt vmcnt(4)
	v_mov_b32_e32 v186, v220
	v_mov_b32_e32 v187, v221
	v_mov_b32_e32 v188, v222
	v_mov_b32_e32 v189, v223
	v_mov_b32_e32 v190, v224
	v_mov_b32_e32 v191, v225
	v_mov_b32_e32 v192, v226
	v_mov_b32_e32 v193, v227
	v_mov_b32_e32 v196, v187
	v_mov_b32_e32 v197, v189
	v_mov_b32_e32 v198, v191
	v_mov_b32_e32 v199, v193
	v_pk_mul_f32 v[194:195], v[48:49], v[196:197]
	v_pk_mul_f32 v[200:201], v[46:47], v[198:199]
	v_mov_b32_e32 v191, v192
	v_mov_b32_e32 v187, v188
	v_pk_fma_f32 v[192:193], v[54:55], v[190:191], v[200:201] neg_lo:[0,0,1] neg_hi:[0,0,1]
	v_pk_fma_f32 v[188:189], v[56:57], v[186:187], v[194:195] neg_lo:[0,0,1] neg_hi:[0,0,1]
	v_pk_mul_f32 v[194:195], v[48:49], v[186:187]
	v_pk_mul_f32 v[200:201], v[46:47], v[190:191]
	v_pk_mul_f32 v[192:193], v[130:131], v[192:193] op_sel_hi:[0,1]
	v_pk_fma_f32 v[200:201], v[54:55], v[198:199], v[200:201]
	v_pk_fma_f32 v[194:195], v[56:57], v[196:197], v[194:195]
	v_pk_mul_f32 v[188:189], v[130:131], v[188:189] op_sel_hi:[0,1]
	v_pk_mul_f32 v[202:203], v[130:131], v[194:195] op_sel_hi:[0,1]
	v_pk_mul_f32 v[194:195], v[130:131], v[200:201] op_sel_hi:[0,1]
	v_cvt_pk_bf16_f32 v192, v192, v193
	v_cvt_pk_bf16_f32 v193, v188, v189
	v_cvt_pk_bf16_f32 v194, v194, v195
	v_cvt_pk_bf16_f32 v195, v202, v203
	global_store_dwordx4 v[172:173], v[192:195], off
	v_pk_mul_f32 v[188:189], v[28:29], v[196:197]
	s_nop 0
	v_pk_mul_f32 v[192:193], v[26:27], v[198:199]
	v_pk_fma_f32 v[188:189], v[36:37], v[186:187], v[188:189] neg_lo:[0,0,1] neg_hi:[0,0,1]
	v_pk_fma_f32 v[192:193], v[34:35], v[190:191], v[192:193] neg_lo:[0,0,1] neg_hi:[0,0,1]
	v_pk_mul_f32 v[186:187], v[28:29], v[186:187]
	v_pk_mul_f32 v[190:191], v[26:27], v[190:191]
	v_pk_mul_f32 v[188:189], v[130:131], v[188:189] op_sel_hi:[0,1]
	v_pk_fma_f32 v[190:191], v[34:35], v[198:199], v[190:191]
	v_pk_fma_f32 v[186:187], v[36:37], v[196:197], v[186:187]
	v_pk_mul_f32 v[192:193], v[130:131], v[192:193] op_sel_hi:[0,1]
	v_pk_mul_f32 v[194:195], v[130:131], v[186:187] op_sel_hi:[0,1]
	v_pk_mul_f32 v[190:191], v[130:131], v[190:191] op_sel_hi:[0,1]
	v_cvt_pk_bf16_f32 v186, v192, v193
	v_cvt_pk_bf16_f32 v187, v188, v189
	v_cvt_pk_bf16_f32 v188, v190, v191
	v_cvt_pk_bf16_f32 v189, v194, v195
	global_store_dwordx4 v[172:173], v[186:189], off offset:256
	v_lshlrev_b64 v[172:173], 8, v[160:161]
	v_lshl_add_u64 v[172:173], v[148:149], 0, v[172:173]
	s_nop 0
	s_nop 0
	v_lshlrev_b64 v[172:173], 11, v[160:161]
	v_lshl_add_u64 v[172:173], v[132:133], 0, v[172:173]
	s_waitcnt vmcnt(2)
	v_mov_b32_e32 v186, v204
	v_mov_b32_e32 v187, v205
	v_mov_b32_e32 v188, v206
	v_mov_b32_e32 v189, v207
	v_mov_b32_e32 v190, v208
	v_mov_b32_e32 v191, v209
	v_mov_b32_e32 v192, v210
	v_mov_b32_e32 v193, v211
	v_mov_b32_e32 v196, v187
	v_mov_b32_e32 v197, v189
	v_mov_b32_e32 v198, v191
	v_mov_b32_e32 v199, v193
	v_pk_mul_f32 v[194:195], v[32:33], v[196:197]
	v_pk_mul_f32 v[200:201], v[30:31], v[198:199]
	v_mov_b32_e32 v191, v192
	v_mov_b32_e32 v187, v188
	v_pk_fma_f32 v[192:193], v[38:39], v[190:191], v[200:201] neg_lo:[0,0,1] neg_hi:[0,0,1]
	v_pk_fma_f32 v[188:189], v[40:41], v[186:187], v[194:195] neg_lo:[0,0,1] neg_hi:[0,0,1]
	v_pk_mul_f32 v[194:195], v[32:33], v[186:187]
	v_pk_mul_f32 v[200:201], v[30:31], v[190:191]
	v_pk_mul_f32 v[192:193], v[130:131], v[192:193] op_sel_hi:[0,1]
	v_pk_fma_f32 v[200:201], v[38:39], v[198:199], v[200:201]
	v_pk_fma_f32 v[194:195], v[40:41], v[196:197], v[194:195]
	v_pk_mul_f32 v[188:189], v[130:131], v[188:189] op_sel_hi:[0,1]
	v_pk_mul_f32 v[202:203], v[130:131], v[194:195] op_sel_hi:[0,1]
	v_pk_mul_f32 v[194:195], v[130:131], v[200:201] op_sel_hi:[0,1]
	v_cvt_pk_bf16_f32 v192, v192, v193
	v_cvt_pk_bf16_f32 v193, v188, v189
	v_cvt_pk_bf16_f32 v194, v194, v195
	v_cvt_pk_bf16_f32 v195, v202, v203
	global_store_dwordx4 v[172:173], v[192:195], off
	v_pk_mul_f32 v[188:189], v[12:13], v[196:197]
	s_nop 0
	v_pk_mul_f32 v[192:193], v[10:11], v[198:199]
	v_pk_fma_f32 v[188:189], v[20:21], v[186:187], v[188:189] neg_lo:[0,0,1] neg_hi:[0,0,1]
	v_pk_fma_f32 v[192:193], v[18:19], v[190:191], v[192:193] neg_lo:[0,0,1] neg_hi:[0,0,1]
	v_pk_mul_f32 v[186:187], v[12:13], v[186:187]
	v_pk_mul_f32 v[190:191], v[10:11], v[190:191]
	v_pk_mul_f32 v[188:189], v[130:131], v[188:189] op_sel_hi:[0,1]
	v_pk_fma_f32 v[190:191], v[18:19], v[198:199], v[190:191]
	v_pk_fma_f32 v[186:187], v[20:21], v[196:197], v[186:187]
	v_pk_mul_f32 v[192:193], v[130:131], v[192:193] op_sel_hi:[0,1]
	v_pk_mul_f32 v[194:195], v[130:131], v[186:187] op_sel_hi:[0,1]
	v_pk_mul_f32 v[190:191], v[130:131], v[190:191] op_sel_hi:[0,1]
	v_cvt_pk_bf16_f32 v186, v192, v193
	v_cvt_pk_bf16_f32 v187, v188, v189
	v_cvt_pk_bf16_f32 v188, v190, v191
	v_cvt_pk_bf16_f32 v189, v194, v195
	global_store_dwordx4 v[172:173], v[186:189], off offset:256
	v_add_u32_e32 v172, 0xb0, v158
	v_ashrrev_i32_e32 v173, 31, v172
	v_lshlrev_b64 v[186:187], 8, v[172:173]
	v_lshl_add_u64 v[190:191], v[148:149], 0, v[186:187]
	s_nop 0
	s_nop 0
	s_nop 0
	v_lshlrev_b64 v[172:173], 11, v[172:173]
	v_lshl_add_u64 v[172:173], v[132:133], 0, v[172:173]
	s_waitcnt vmcnt(0)
	v_mov_b32_e32 v186, v212
	v_mov_b32_e32 v187, v213
	v_mov_b32_e32 v188, v214
	v_mov_b32_e32 v189, v215
	v_mov_b32_e32 v190, v216
	v_mov_b32_e32 v191, v217
	v_mov_b32_e32 v192, v218
	v_mov_b32_e32 v193, v219
	v_mov_b32_e32 v132, v187
	v_mov_b32_e32 v133, v189
	v_mov_b32_e32 v196, v191
	v_mov_b32_e32 v197, v193
	v_pk_mul_f32 v[194:195], v[16:17], v[132:133]
	v_pk_mul_f32 v[198:199], v[14:15], v[196:197]
	v_mov_b32_e32 v191, v192
	v_mov_b32_e32 v187, v188
	v_pk_fma_f32 v[192:193], v[22:23], v[190:191], v[198:199] neg_lo:[0,0,1] neg_hi:[0,0,1]
	v_pk_fma_f32 v[188:189], v[24:25], v[186:187], v[194:195] neg_lo:[0,0,1] neg_hi:[0,0,1]
	v_pk_mul_f32 v[194:195], v[16:17], v[186:187]
	v_pk_mul_f32 v[198:199], v[14:15], v[190:191]
	v_pk_mul_f32 v[192:193], v[130:131], v[192:193] op_sel_hi:[0,1]
	v_pk_fma_f32 v[198:199], v[22:23], v[196:197], v[198:199]
	v_pk_fma_f32 v[194:195], v[24:25], v[132:133], v[194:195]
	v_pk_mul_f32 v[188:189], v[130:131], v[188:189] op_sel_hi:[0,1]
	v_pk_mul_f32 v[200:201], v[130:131], v[194:195] op_sel_hi:[0,1]
	v_pk_mul_f32 v[194:195], v[130:131], v[198:199] op_sel_hi:[0,1]
	v_cvt_pk_bf16_f32 v192, v192, v193
	v_cvt_pk_bf16_f32 v193, v188, v189
	v_cvt_pk_bf16_f32 v194, v194, v195
	v_cvt_pk_bf16_f32 v195, v200, v201
	global_store_dwordx4 v[172:173], v[192:195], off
	v_pk_mul_f32 v[188:189], v[4:5], v[132:133]
	s_nop 0
	v_pk_mul_f32 v[192:193], v[2:3], v[196:197]
	v_pk_fma_f32 v[188:189], v[8:9], v[186:187], v[188:189] neg_lo:[0,0,1] neg_hi:[0,0,1]
	v_pk_fma_f32 v[192:193], v[6:7], v[190:191], v[192:193] neg_lo:[0,0,1] neg_hi:[0,0,1]
	v_pk_mul_f32 v[186:187], v[4:5], v[186:187]
	v_pk_mul_f32 v[190:191], v[2:3], v[190:191]
	v_pk_fma_f32 v[132:133], v[8:9], v[132:133], v[186:187]
	v_pk_fma_f32 v[190:191], v[6:7], v[196:197], v[190:191]
	v_pk_mul_f32 v[186:187], v[130:131], v[132:133] op_sel_hi:[0,1]
	v_pk_mul_f32 v[132:133], v[130:131], v[190:191] op_sel_hi:[0,1]
	v_pk_mul_f32 v[188:189], v[130:131], v[188:189] op_sel_hi:[0,1]
	v_pk_mul_f32 v[192:193], v[130:131], v[192:193] op_sel_hi:[0,1]
	v_cvt_pk_bf16_f32 v130, v192, v193
	v_cvt_pk_bf16_f32 v131, v188, v189
	v_cvt_pk_bf16_f32 v132, v132, v133
	v_cvt_pk_bf16_f32 v133, v186, v187
	s_cbranch_execnz .LBB0_131
